# speedup vs baseline: 1.0028x; 1.0023x over previous
.LBB4_39:
	s_or_b64 exec, exec, s[32:33]
	s_setprio 1
	ds_read_b128 v[26:29], v86
	ds_read_b128 v[30:33], v86 offset:1024
	ds_read_b128 v[106:109], v86 offset:2048
	ds_read_b128 v[110:113], v86 offset:3072
	s_waitcnt lgkmcnt(2)
	v_mfma_f32_16x16x32_f16 v[34:37], v[26:29], v[40:43], 0
	v_mfma_f32_16x16x32_f16 v[114:117], v[26:29], v[48:51], 0
	v_mfma_f32_16x16x32_f16 v[118:121], v[26:29], v[56:59], 0
	v_mfma_f32_16x16x32_f16 v[34:37], v[30:33], v[44:47], v[34:37]
	v_mfma_f32_16x16x32_f16 v[114:117], v[30:33], v[52:55], v[114:117]
	v_mfma_f32_16x16x32_f16 v[118:121], v[30:33], v[60:63], v[118:121]
	s_waitcnt lgkmcnt(0)
	v_mfma_f32_16x16x32_f16 v[122:125], v[106:109], v[40:43], 0
	v_mfma_f32_16x16x32_f16 v[122:125], v[110:113], v[44:47], v[122:125]
	s_add_u32 s16, s20, s0
	s_addc_u32 s17, s21, s1
	s_load_dwordx8 s[36:43], s[16:17], 0x16900
	s_load_dwordx8 s[44:51], s[16:17], 0x16920
	s_load_dwordx8 s[52:59], s[16:17], 0x16940
	s_load_dwordx8 s[60:67], s[16:17], 0x16960
	s_load_dwordx4 s[68:71], s[16:17], 0x16980
	s_load_dwordx8 s[72:79], s[16:17], 0x16b40
	s_load_dwordx8 s[80:87], s[16:17], 0x16b60
	s_load_dwordx8 s[88:95], s[16:17], 0x16b80
	s_load_dwordx4 s[96:99], s[16:17], 0x16ba0
	s_load_dwordx8 s[8:15], s[16:17], 0x16bb0
	s_nop 2
	v_cvt_pk_f16_f32 v34, v34, v35
	v_cvt_pk_f16_f32 v35, v36, v37
	ds_write_b64 v88, v[34:35]
	v_cvt_pk_f16_f32 v114, v114, v115
	v_cvt_pk_f16_f32 v115, v116, v117
	ds_write_b64 v90, v[114:115]
	v_cvt_pk_f16_f32 v118, v118, v119
	v_cvt_pk_f16_f32 v119, v120, v121
	ds_write_b64 v92, v[118:119]
	v_mfma_f32_16x16x32_f16 v[34:37], v[106:109], v[48:51], 0
	v_mfma_f32_16x16x32_f16 v[114:117], v[106:109], v[56:59], 0
	v_mfma_f32_16x16x32_f16 v[34:37], v[110:113], v[52:55], v[34:37]
	v_mfma_f32_16x16x32_f16 v[114:117], v[110:113], v[60:63], v[114:117]
	v_cvt_pk_f16_f32 v122, v122, v123
	v_cvt_pk_f16_f32 v123, v124, v125
	ds_write_b64 v88, v[122:123] offset:32
	s_nop 3
	v_cvt_pk_f16_f32 v34, v34, v35
	v_cvt_pk_f16_f32 v35, v36, v37
	ds_write_b64 v90, v[34:35] offset:32
	v_cvt_pk_f16_f32 v114, v114, v115
	v_cvt_pk_f16_f32 v115, v116, v117
	ds_write_b64 v92, v[114:115] offset:32
	s_setprio 0
	s_waitcnt lgkmcnt(0)
	s_barrier
	v_add_u32_e32 v105, s25, v80
	ds_read_b128 v[30:33], v105
	ds_read_b128 v[34:37], v105 offset:64
	ds_read_b128 v[106:109], v105 offset:144
	ds_read_b128 v[110:113], v105 offset:208
	ds_read_b128 v[114:117], v105 offset:288
	ds_read_b128 v[122:125], v105 offset:352
	s_waitcnt lgkmcnt(4)
	v_pk_fma_f16 v118, v30, s36, 0
	v_pk_fma_f16 v119, v31, s37, 0
	v_pk_fma_f16 v120, v32, s38, 0
	v_pk_fma_f16 v121, v33, s39, 0
	v_pk_fma_f16 v26, v34, s72, 0
	v_pk_fma_f16 v27, v35, s73, 0
	v_pk_fma_f16 v28, v36, s74, 0
	v_pk_fma_f16 v29, v37, s75, 0
	ds_read_b128 v[30:33], v105 offset:2592
	ds_read_b128 v[34:37], v105 offset:2656
	s_waitcnt lgkmcnt(4)
	v_pk_fma_f16 v118, v106, s40, v118
	v_pk_fma_f16 v119, v107, s41, v119
	v_pk_fma_f16 v120, v108, s42, v120
	v_pk_fma_f16 v121, v109, s43, v121
	v_pk_fma_f16 v26, v110, s76, v26
	v_pk_fma_f16 v27, v111, s77, v27
	v_pk_fma_f16 v28, v112, s78, v28
	v_pk_fma_f16 v29, v113, s79, v29
	ds_read_b128 v[106:109], v105 offset:2736
	ds_read_b128 v[110:113], v105 offset:2800
	s_waitcnt lgkmcnt(4)
	v_pk_fma_f16 v118, v114, s44, v118
	v_pk_fma_f16 v119, v115, s45, v119
	v_pk_fma_f16 v120, v116, s46, v120
	v_pk_fma_f16 v121, v117, s47, v121
	v_pk_fma_f16 v26, v122, s80, v26
	v_pk_fma_f16 v27, v123, s81, v27
	v_pk_fma_f16 v28, v124, s82, v28
	v_pk_fma_f16 v29, v125, s83, v29
	ds_read_b128 v[114:117], v105 offset:2880
	ds_read_b128 v[122:125], v105 offset:2944
	s_waitcnt lgkmcnt(4)
	v_pk_fma_f16 v118, v30, s48, v118
	v_pk_fma_f16 v119, v31, s49, v119
	v_pk_fma_f16 v120, v32, s50, v120
	v_pk_fma_f16 v121, v33, s51, v121
	v_pk_fma_f16 v26, v34, s84, v26
	v_pk_fma_f16 v27, v35, s85, v27
	v_pk_fma_f16 v28, v36, s86, v28
	v_pk_fma_f16 v29, v37, s87, v29
	ds_read_b128 v[30:33], v105 offset:5184
	ds_read_b128 v[34:37], v105 offset:5248
	s_waitcnt lgkmcnt(4)
	v_pk_fma_f16 v118, v106, s52, v118
	v_pk_fma_f16 v119, v107, s53, v119
	v_pk_fma_f16 v120, v108, s54, v120
	v_pk_fma_f16 v121, v109, s55, v121
	v_pk_fma_f16 v26, v110, s88, v26
	v_pk_fma_f16 v27, v111, s89, v27
	v_pk_fma_f16 v28, v112, s90, v28
	v_pk_fma_f16 v29, v113, s91, v29
	ds_read_b128 v[106:109], v105 offset:5328
	ds_read_b128 v[110:113], v105 offset:5392
	s_waitcnt lgkmcnt(4)
	v_pk_fma_f16 v118, v114, s56, v118
	v_pk_fma_f16 v119, v115, s57, v119
	v_pk_fma_f16 v120, v116, s58, v120
	v_pk_fma_f16 v121, v117, s59, v121
	v_pk_fma_f16 v26, v122, s92, v26
	v_pk_fma_f16 v27, v123, s93, v27
	v_pk_fma_f16 v28, v124, s94, v28
	v_pk_fma_f16 v29, v125, s95, v29
	ds_read_b128 v[114:117], v105 offset:5472
	ds_read_b128 v[122:125], v105 offset:5536
	s_waitcnt lgkmcnt(4)
	v_pk_fma_f16 v118, v30, s60, v118
	v_pk_fma_f16 v119, v31, s61, v119
	v_pk_fma_f16 v120, v32, s62, v120
	v_pk_fma_f16 v121, v33, s63, v121
	v_pk_fma_f16 v26, v34, s96, v26
	v_pk_fma_f16 v27, v35, s97, v27
	v_pk_fma_f16 v28, v36, s98, v28
	v_pk_fma_f16 v29, v37, s99, v29
	s_waitcnt lgkmcnt(2)
	v_pk_fma_f16 v118, v106, s64, v118
	v_pk_fma_f16 v119, v107, s65, v119
	v_pk_fma_f16 v120, v108, s66, v120
	v_pk_fma_f16 v121, v109, s67, v121
	v_pk_fma_f16 v26, v110, s8, v26
	v_pk_fma_f16 v27, v111, s9, v27
	v_pk_fma_f16 v28, v112, s10, v28
	v_pk_fma_f16 v29, v113, s11, v29
	s_waitcnt lgkmcnt(0)
	v_pk_fma_f16 v26, v122, s12, v26
	v_pk_fma_f16 v27, v123, s13, v27
	v_pk_fma_f16 v28, v124, s14, v28
	v_pk_fma_f16 v29, v125, s15, v29
	v_pk_fma_f16 v109, v114, s68, v118
	v_pk_fma_f16 v123, v115, s69, v119
	v_pk_fma_f16 v122, v116, s70, v120
	v_pk_fma_f16 v105, v117, s71, v121
	v_mov_b64_e32 v[114:115], s[22:23]
	v_fma_mix_f32 v106, |v109|, s31, v104 op_sel_hi:[1,0,0]
	v_fma_mix_f32 v107, |v109|, s31, v104 op_sel:[1,0,0] op_sel_hi:[1,0,0]
	v_rcp_f32_e32 v106, v106
	v_rcp_f32_e32 v107, v107
	v_fma_mix_f32 v110, v109, s100, 0 op_sel_hi:[1,0,0]
	v_fma_mix_f32 v111, v109, s100, 0 op_sel:[1,0,0] op_sel_hi:[1,0,0]
	v_mul_f32_e64 v110, v110, -v110
	v_mul_f32_e64 v111, v111, -v111
	v_pk_fma_f32 v[116:117], v[106:107], s[24:25], v[114:115] op_sel_hi:[1,0,0]
	v_exp_f32_e32 v110, v110
	v_pk_fma_f32 v[116:117], v[116:117], v[106:107], s[26:27] op_sel_hi:[1,1,0]
	v_exp_f32_e32 v111, v111
	v_pk_fma_f32 v[116:117], v[116:117], v[106:107], s[28:29] op_sel_hi:[1,1,0]
	v_pk_max_f16 v112, v109, 0
	v_pk_fma_f32 v[116:117], v[116:117], v[106:107], s[30:31] op_sel_hi:[1,1,0]
	v_pk_mul_f32 v[106:107], v[106:107], v[116:117]
	v_pk_mul_f32 v[106:107], v[110:111], v[106:107]
	v_fma_mixlo_f16 v109, -|v109|, v106, v112 op_sel_hi:[1,0,1]
	v_fma_mixhi_f16 v109, -|v109|, v107, v112 op_sel:[1,0,1] op_sel_hi:[1,0,1]
	v_fma_mix_f32 v106, |v123|, s31, v104 op_sel_hi:[1,0,0]
	v_fma_mix_f32 v107, |v123|, s31, v104 op_sel:[1,0,0] op_sel_hi:[1,0,0]
	v_rcp_f32_e32 v106, v106
	v_rcp_f32_e32 v107, v107
	v_fma_mix_f32 v110, v123, s100, 0 op_sel_hi:[1,0,0]
	v_fma_mix_f32 v111, v123, s100, 0 op_sel:[1,0,0] op_sel_hi:[1,0,0]
	v_mul_f32_e64 v110, v110, -v110
	v_mul_f32_e64 v111, v111, -v111
	v_pk_fma_f32 v[116:117], v[106:107], s[24:25], v[114:115] op_sel_hi:[1,0,0]
	v_exp_f32_e32 v110, v110
	v_pk_fma_f32 v[116:117], v[116:117], v[106:107], s[26:27] op_sel_hi:[1,1,0]
	v_exp_f32_e32 v111, v111
	v_pk_fma_f32 v[116:117], v[116:117], v[106:107], s[28:29] op_sel_hi:[1,1,0]
	v_pk_max_f16 v112, v123, 0
	v_pk_fma_f32 v[116:117], v[116:117], v[106:107], s[30:31] op_sel_hi:[1,1,0]
	v_pk_mul_f32 v[106:107], v[106:107], v[116:117]
	v_pk_mul_f32 v[106:107], v[110:111], v[106:107]
	v_fma_mixlo_f16 v123, -|v123|, v106, v112 op_sel_hi:[1,0,1]
	v_fma_mixhi_f16 v123, -|v123|, v107, v112 op_sel:[1,0,1] op_sel_hi:[1,0,1]
	v_fma_mix_f32 v106, |v122|, s31, v104 op_sel_hi:[1,0,0]
	v_fma_mix_f32 v107, |v122|, s31, v104 op_sel:[1,0,0] op_sel_hi:[1,0,0]
	v_rcp_f32_e32 v106, v106
	v_rcp_f32_e32 v107, v107
	v_fma_mix_f32 v110, v122, s100, 0 op_sel_hi:[1,0,0]
	v_fma_mix_f32 v111, v122, s100, 0 op_sel:[1,0,0] op_sel_hi:[1,0,0]
	v_mul_f32_e64 v110, v110, -v110
	v_mul_f32_e64 v111, v111, -v111
	v_pk_fma_f32 v[116:117], v[106:107], s[24:25], v[114:115] op_sel_hi:[1,0,0]
	v_exp_f32_e32 v110, v110
	v_pk_fma_f32 v[116:117], v[116:117], v[106:107], s[26:27] op_sel_hi:[1,1,0]
	v_exp_f32_e32 v111, v111
	v_pk_fma_f32 v[116:117], v[116:117], v[106:107], s[28:29] op_sel_hi:[1,1,0]
	v_pk_max_f16 v112, v122, 0
	v_pk_fma_f32 v[116:117], v[116:117], v[106:107], s[30:31] op_sel_hi:[1,1,0]
	v_pk_mul_f32 v[106:107], v[106:107], v[116:117]
	v_pk_mul_f32 v[106:107], v[110:111], v[106:107]
	v_fma_mixlo_f16 v122, -|v122|, v106, v112 op_sel_hi:[1,0,1]
	v_fma_mixhi_f16 v122, -|v122|, v107, v112 op_sel:[1,0,1] op_sel_hi:[1,0,1]
	v_fma_mix_f32 v106, |v105|, s31, v104 op_sel_hi:[1,0,0]
	v_fma_mix_f32 v107, |v105|, s31, v104 op_sel:[1,0,0] op_sel_hi:[1,0,0]
	v_rcp_f32_e32 v106, v106
	v_rcp_f32_e32 v107, v107
	v_fma_mix_f32 v110, v105, s100, 0 op_sel_hi:[1,0,0]
	v_fma_mix_f32 v111, v105, s100, 0 op_sel:[1,0,0] op_sel_hi:[1,0,0]
	v_mul_f32_e64 v110, v110, -v110
	v_mul_f32_e64 v111, v111, -v111
	v_pk_fma_f32 v[116:117], v[106:107], s[24:25], v[114:115] op_sel_hi:[1,0,0]
	v_exp_f32_e32 v110, v110
	v_pk_fma_f32 v[116:117], v[116:117], v[106:107], s[26:27] op_sel_hi:[1,1,0]
	v_exp_f32_e32 v111, v111
	v_pk_fma_f32 v[116:117], v[116:117], v[106:107], s[28:29] op_sel_hi:[1,1,0]
	v_pk_max_f16 v112, v105, 0
	v_pk_fma_f32 v[116:117], v[116:117], v[106:107], s[30:31] op_sel_hi:[1,1,0]
	v_pk_mul_f32 v[106:107], v[106:107], v[116:117]
	v_pk_mul_f32 v[106:107], v[110:111], v[106:107]
	v_fma_mixlo_f16 v105, -|v105|, v106, v112 op_sel_hi:[1,0,1]
	v_fma_mixhi_f16 v105, -|v105|, v107, v112 op_sel:[1,0,1] op_sel_hi:[1,0,1]
	v_pk_mul_f16 v26, v26, v109
	v_pk_mul_f16 v27, v27, v123
	v_pk_mul_f16 v28, v28, v122
	s_nop 0
	v_pk_mul_f16 v29, v29, v105
	v_add_u32_e32 v30, s25, v78
	ds_write_b128 v30, v[26:29]
	s_waitcnt vmcnt(0)
	ds_write_b128 v39, v[22:25]
	s_and_saveexec_b64 s[32:33], s[4:5]
	s_cbranch_execz .LBB4_36
	ds_write_b128 v39, v[18:21] offset:8192
	s_branch .LBB4_36
